# DSA attention P@V: all V index reads in one burst, six V gather batches in flight instead of two (on top of v42)
# speedup vs baseline: 1.0055x; 1.0019x over previous
.LBB0_1334:
	v_and_b32_e32 v34, 64, v209
	v_xor_b32_e32 v18, 16, v209
	v_add_u32_e32 v19, 64, v34
	v_cmp_lt_i32_e32 vcc, v18, v19
	v_max_f32_e32 v21, v215, v215
	v_mov_b32_e32 v32, v141
	v_cndmask_b32_e32 v18, v209, v18, vcc
	v_lshlrev_b32_e32 v18, 2, v18
	ds_bpermute_b32 v20, v18, v215
	v_mov_b32_e32 v33, v141
	v_readlane_b32 s9, v254, 54
	s_movk_i32 s8, 0x520
	v_lshlrev_b32_e32 v34, 2, v34
	s_waitcnt lgkmcnt(0)
	v_max_f32_e32 v20, v20, v20
	v_max_f32_e32 v20, v21, v20
	v_xor_b32_e32 v21, 32, v209
	v_cmp_lt_i32_e32 vcc, v21, v19
	s_lshl_b64 s[0:1], s[0:1], 9
	s_lshl_b64 s[0:1], s[0:1], 1
	v_cndmask_b32_e32 v19, v209, v21, vcc
	v_lshlrev_b32_e32 v19, 2, v19
	ds_bpermute_b32 v21, v19, v20
	s_waitcnt lgkmcnt(0)
	v_max_f32_e32 v21, v21, v21
	v_max_f32_e32 v20, v20, v21
	v_add_f32_e32 v20, 0xc1000000, v20
	v_sub_f32_e32 v21, v118, v20
	v_exp_f32_e32 v21, v21
	v_sub_f32_e32 v23, v119, v20
	v_exp_f32_e32 v23, v23
	v_sub_f32_e32 v24, v120, v20
	v_exp_f32_e32 v24, v24
	v_sub_f32_e32 v25, v121, v20
	v_exp_f32_e32 v25, v25
	v_sub_f32_e32 v26, v122, v20
	v_add_f32_e32 v22, 0, v21
	v_exp_f32_e32 v26, v26
	v_sub_f32_e32 v27, v123, v20
	v_add_f32_e32 v22, v23, v22
	v_exp_f32_e32 v27, v27
	v_sub_f32_e32 v28, v124, v20
	v_add_f32_e32 v22, v24, v22
	v_exp_f32_e32 v28, v28
	v_sub_f32_e32 v29, v125, v20
	v_add_f32_e32 v22, v25, v22
	v_exp_f32_e32 v29, v29
	v_sub_f32_e32 v30, v126, v20
	v_add_f32_e32 v22, v26, v22
	v_exp_f32_e32 v31, v30
	v_sub_f32_e32 v30, v127, v20
	v_add_f32_e32 v22, v27, v22
	v_exp_f32_e32 v36, v30
	v_sub_f32_e32 v30, v128, v20
	v_add_f32_e32 v22, v28, v22
	v_exp_f32_e32 v37, v30
	v_sub_f32_e32 v30, v129, v20
	v_add_f32_e32 v22, v29, v22
	v_exp_f32_e32 v38, v30
	v_sub_f32_e32 v30, v130, v20
	v_add_f32_e32 v22, v31, v22
	v_exp_f32_e32 v39, v30
	v_sub_f32_e32 v30, v131, v20
	v_add_f32_e32 v22, v36, v22
	v_exp_f32_e32 v40, v30
	v_sub_f32_e32 v30, v132, v20
	v_add_f32_e32 v22, v37, v22
	v_exp_f32_e32 v41, v30
	v_sub_f32_e32 v30, v133, v20
	v_add_f32_e32 v22, v38, v22
	v_exp_f32_e32 v42, v30
	v_sub_f32_e32 v30, v134, v20
	v_add_f32_e32 v22, v39, v22
	v_exp_f32_e32 v43, v30
	v_sub_f32_e32 v30, v135, v20
	v_add_f32_e32 v22, v40, v22
	v_exp_f32_e32 v44, v30
	v_sub_f32_e32 v30, v136, v20
	v_add_f32_e32 v22, v41, v22
	v_exp_f32_e32 v45, v30
	v_sub_f32_e32 v30, v137, v20
	v_add_f32_e32 v22, v42, v22
	v_exp_f32_e32 v46, v30
	v_sub_f32_e32 v30, v156, v20
	v_add_f32_e32 v22, v43, v22
	v_exp_f32_e32 v47, v30
	v_sub_f32_e32 v30, v157, v20
	v_add_f32_e32 v22, v44, v22
	v_exp_f32_e32 v48, v30
	v_sub_f32_e32 v30, v158, v20
	v_add_f32_e32 v22, v45, v22
	v_exp_f32_e32 v49, v30
	v_sub_f32_e32 v30, v159, v20
	v_add_f32_e32 v22, v46, v22
	v_exp_f32_e32 v50, v30
	v_sub_f32_e32 v30, v160, v20
	v_add_f32_e32 v22, v47, v22
	v_exp_f32_e32 v51, v30
	v_sub_f32_e32 v30, v161, v20
	v_add_f32_e32 v22, v48, v22
	v_exp_f32_e32 v52, v30
	v_sub_f32_e32 v30, v162, v20
	v_add_f32_e32 v22, v49, v22
	v_exp_f32_e32 v53, v30
	v_sub_f32_e32 v30, v163, v20
	v_add_f32_e32 v22, v50, v22
	v_exp_f32_e32 v54, v30
	v_sub_f32_e32 v30, v164, v20
	v_add_f32_e32 v22, v51, v22
	v_exp_f32_e32 v55, v30
	v_sub_f32_e32 v30, v165, v20
	v_add_f32_e32 v22, v52, v22
	v_exp_f32_e32 v56, v30
	v_sub_f32_e32 v30, v166, v20
	v_add_f32_e32 v22, v53, v22
	v_exp_f32_e32 v57, v30
	v_sub_f32_e32 v30, v167, v20
	v_add_f32_e32 v22, v54, v22
	v_exp_f32_e32 v58, v30
	v_sub_f32_e32 v30, v168, v20
	v_add_f32_e32 v22, v55, v22
	v_exp_f32_e32 v59, v30
	v_sub_f32_e32 v30, v169, v20
	v_add_f32_e32 v22, v56, v22
	v_exp_f32_e32 v60, v30
	v_sub_f32_e32 v30, v170, v20
	v_add_f32_e32 v22, v57, v22
	v_exp_f32_e32 v61, v30
	v_sub_f32_e32 v30, v171, v20
	v_add_f32_e32 v22, v58, v22
	v_exp_f32_e32 v62, v30
	v_sub_f32_e32 v30, v172, v20
	v_add_f32_e32 v22, v59, v22
	v_exp_f32_e32 v63, v30
	v_sub_f32_e32 v30, v173, v20
	v_add_f32_e32 v22, v60, v22
	v_exp_f32_e32 v64, v30
	v_sub_f32_e32 v30, v174, v20
	v_add_f32_e32 v22, v61, v22
	v_exp_f32_e32 v65, v30
	v_sub_f32_e32 v30, v175, v20
	v_add_f32_e32 v22, v62, v22
	v_exp_f32_e32 v66, v30
	v_sub_f32_e32 v30, v176, v20
	v_add_f32_e32 v22, v63, v22
	v_exp_f32_e32 v67, v30
	v_sub_f32_e32 v30, v177, v20
	v_add_f32_e32 v22, v64, v22
	v_exp_f32_e32 v68, v30
	v_sub_f32_e32 v30, v178, v20
	v_add_f32_e32 v22, v65, v22
	v_exp_f32_e32 v69, v30
	v_sub_f32_e32 v30, v179, v20
	v_add_f32_e32 v22, v66, v22
	v_exp_f32_e32 v70, v30
	v_sub_f32_e32 v30, v180, v20
	v_add_f32_e32 v22, v67, v22
	v_exp_f32_e32 v71, v30
	v_sub_f32_e32 v30, v181, v20
	v_add_f32_e32 v22, v68, v22
	v_exp_f32_e32 v72, v30
	v_sub_f32_e32 v30, v182, v20
	v_add_f32_e32 v22, v69, v22
	v_exp_f32_e32 v73, v30
	v_sub_f32_e32 v30, v183, v20
	v_add_f32_e32 v22, v70, v22
	v_exp_f32_e32 v74, v30
	v_sub_f32_e32 v30, v184, v20
	v_add_f32_e32 v22, v71, v22
	v_exp_f32_e32 v75, v30
	v_sub_f32_e32 v30, v185, v20
	v_add_f32_e32 v22, v72, v22
	v_exp_f32_e32 v76, v30
	v_sub_f32_e32 v30, v186, v20
	v_add_f32_e32 v22, v73, v22
	v_exp_f32_e32 v77, v30
	v_sub_f32_e32 v30, v187, v20
	v_add_f32_e32 v22, v74, v22
	v_exp_f32_e32 v78, v30
	v_sub_f32_e32 v30, v188, v20
	v_add_f32_e32 v22, v75, v22
	v_exp_f32_e32 v79, v30
	v_sub_f32_e32 v30, v189, v20
	v_add_f32_e32 v22, v76, v22
	v_exp_f32_e32 v80, v30
	v_sub_f32_e32 v30, v190, v20
	v_add_f32_e32 v22, v77, v22
	v_exp_f32_e32 v81, v30
	v_sub_f32_e32 v30, v191, v20
	v_add_f32_e32 v22, v78, v22
	v_exp_f32_e32 v82, v30
	v_sub_f32_e32 v30, v192, v20
	v_add_f32_e32 v22, v79, v22
	v_exp_f32_e32 v83, v30
	v_sub_f32_e32 v30, v193, v20
	v_add_f32_e32 v22, v80, v22
	v_exp_f32_e32 v84, v30
	v_sub_f32_e32 v30, v194, v20
	v_add_f32_e32 v22, v81, v22
	v_exp_f32_e32 v85, v30
	v_sub_f32_e32 v30, v195, v20
	v_add_f32_e32 v22, v82, v22
	v_exp_f32_e32 v86, v30
	v_sub_f32_e32 v30, v196, v20
	v_add_f32_e32 v22, v83, v22
	v_exp_f32_e32 v87, v30
	v_sub_f32_e32 v30, v197, v20
	v_add_f32_e32 v22, v84, v22
	v_exp_f32_e32 v88, v30
	v_sub_f32_e32 v30, v198, v20
	v_add_f32_e32 v22, v85, v22
	v_exp_f32_e32 v89, v30
	v_sub_f32_e32 v20, v199, v20
	v_add_f32_e32 v22, v86, v22
	v_exp_f32_e32 v90, v20
	v_add_f32_e32 v22, v87, v22
	v_add_f32_e32 v22, v88, v22
	v_add_f32_e32 v22, v89, v22
	v_add_f32_e32 v20, v90, v22
	ds_bpermute_b32 v18, v18, v20
	v_cvt_pk_fp8_f32 v32, v21, v23
	v_cvt_pk_fp8_f32 v33, v26, v27
	v_mov_b32_e32 v30, v141
	v_cvt_pk_fp8_f32 v30, v31, v36
	s_waitcnt lgkmcnt(0)
	v_add_f32_e32 v18, v20, v18
	ds_bpermute_b32 v19, v19, v18
	v_cvt_pk_fp8_f32 v32, v24, v25 op_sel:[0,0,1]
	v_cvt_pk_fp8_f32 v33, v28, v29 op_sel:[0,0,1]
	v_mov_b32_e32 v31, v141
	v_mov_b32_e32 v28, v141
	s_waitcnt lgkmcnt(0)
	v_add_f32_e32 v35, v18, v19
	v_mov_b32_e32 v29, v141
	v_mov_b32_e32 v24, v141
	v_mov_b32_e32 v25, v141
	v_mov_b32_e32 v22, v141
	v_mov_b32_e32 v23, v141
	v_mov_b32_e32 v20, v141
	v_mov_b32_e32 v21, v141
	v_mov_b32_e32 v18, v141
	v_mov_b32_e32 v19, v141
	v_mov_b32_e32 v26, v141
	v_mov_b32_e32 v27, v141
	v_cvt_pk_fp8_f32 v31, v39, v40
	v_cvt_pk_fp8_f32 v28, v43, v44
	v_cvt_pk_fp8_f32 v29, v47, v48
	v_cvt_pk_fp8_f32 v24, v51, v52
	v_cvt_pk_fp8_f32 v25, v55, v56
	v_cvt_pk_fp8_f32 v22, v59, v60
	v_cvt_pk_fp8_f32 v23, v63, v64
	v_cvt_pk_fp8_f32 v20, v67, v68
	v_cvt_pk_fp8_f32 v21, v71, v72
	v_cvt_pk_fp8_f32 v18, v75, v76
	v_cvt_pk_fp8_f32 v19, v79, v80
	v_cvt_pk_fp8_f32 v26, v83, v84
	v_cvt_pk_fp8_f32 v27, v87, v88
	v_cvt_pk_fp8_f32 v30, v37, v38 op_sel:[0,0,1]
	v_cvt_pk_fp8_f32 v31, v41, v42 op_sel:[0,0,1]
	v_cvt_pk_fp8_f32 v28, v45, v46 op_sel:[0,0,1]
	v_cvt_pk_fp8_f32 v29, v49, v50 op_sel:[0,0,1]
	v_cvt_pk_fp8_f32 v24, v53, v54 op_sel:[0,0,1]
	v_cvt_pk_fp8_f32 v25, v57, v58 op_sel:[0,0,1]
	v_cvt_pk_fp8_f32 v22, v61, v62 op_sel:[0,0,1]
	v_cvt_pk_fp8_f32 v23, v65, v66 op_sel:[0,0,1]
	v_cvt_pk_fp8_f32 v20, v69, v70 op_sel:[0,0,1]
	v_cvt_pk_fp8_f32 v21, v73, v74 op_sel:[0,0,1]
	v_cvt_pk_fp8_f32 v18, v77, v78 op_sel:[0,0,1]
	v_cvt_pk_fp8_f32 v19, v81, v82 op_sel:[0,0,1]
	v_cvt_pk_fp8_f32 v26, v85, v86 op_sel:[0,0,1]
	v_cvt_pk_fp8_f32 v27, v89, v90 op_sel:[0,0,1]
	s_nop 0
	ds_read_u16 v86, v212 offset:64
	ds_read_u16 v87, v212 offset:80
	ds_read_u16 v88, v212 offset:96
	ds_read_u16 v89, v212 offset:112
	ds_read_u16 v90, v212 offset:128
	ds_read_u16 v91, v212 offset:144
	ds_read_u16 v92, v212 offset:160
	ds_read_u16 v93, v212 offset:176
	ds_read_u16 v94, v212 offset:192
	ds_read_u16 v95, v212 offset:208
	ds_read_u16 v96, v212 offset:224
	ds_read_u16 v97, v212 offset:240
	ds_read_u16 v98, v212 offset:256
	ds_read_u16 v99, v212 offset:272
	ds_read_u16 v100, v212 offset:288
	ds_read_u16 v101, v212 offset:304
	ds_read_u16 v102, v212 offset:320
	ds_read_u16 v103, v212 offset:336
	ds_read_u16 v104, v212 offset:352
	ds_read_u16 v105, v212 offset:368
	ds_read_u16 v106, v212 offset:384
	ds_read_u16 v107, v212 offset:400
	ds_read_u16 v108, v212 offset:416
	ds_read_u16 v109, v212 offset:432
	ds_read_u16 v110, v212 offset:448
	ds_read_u16 v111, v212 offset:464
	ds_read_u16 v112, v212 offset:480
	ds_read_u16 v113, v212 offset:496
	v_ashrrev_i32_e32 v36, 1, v210
	v_cmp_gt_i32_e32 vcc, 4, v36
	v_add_u32_e32 v37, 12, v117
	v_mov_b32_e32 v54, s9
	v_cndmask_b32_e32 v37, v37, v117, vcc
	v_add_u32_e32 v36, v37, v36
	v_and_b32_e32 v37, 15, v36
	v_mad_u32_u24 v37, v37, s24, v54
	v_lshrrev_b32_e32 v36, 4, v36
	v_lshlrev_b32_e32 v54, 3, v210
	v_mul_lo_u32 v36, v36, s8
	v_and_b32_e32 v54, 8, v54
	v_add3_u32 v36, v37, v36, v54
	v_lshrrev_b32_e32 v37, 2, v214
	s_movk_i32 s8, 0xa40
	v_mul_lo_u32 v37, v37, s8
	v_add_u32_e32 v37, s9, v37
	v_and_b32_e32 v54, 48, v116
	v_mul_lo_u32 v55, v213, s24
	v_add3_u32 v37, v37, v54, v55
	s_waitcnt lgkmcnt(0)
	v_lshlrev_b32_e32 v140, 7, v86
	v_lshl_add_u64 v[244:245], v[114:115], 0, v[140:141]
	global_load_dwordx4 v[38:41], v[244:245], off
	v_lshlrev_b32_e32 v140, 7, v87
	v_lshl_add_u64 v[246:247], v[114:115], 0, v[140:141]
	global_load_dwordx4 v[42:45], v[246:247], off
	v_lshlrev_b32_e32 v140, 7, v88
	v_lshl_add_u64 v[248:249], v[114:115], 0, v[140:141]
	global_load_dwordx4 v[46:49], v[248:249], off
	v_lshlrev_b32_e32 v140, 7, v89
	v_lshl_add_u64 v[250:251], v[114:115], 0, v[140:141]
	global_load_dwordx4 v[50:53], v[250:251], off
	v_lshlrev_b32_e32 v140, 7, v90
	v_lshl_add_u64 v[244:245], v[114:115], 0, v[140:141]
	global_load_dwordx4 v[156:159], v[244:245], off
	v_lshlrev_b32_e32 v140, 7, v91
	v_lshl_add_u64 v[246:247], v[114:115], 0, v[140:141]
	global_load_dwordx4 v[160:163], v[246:247], off
	v_lshlrev_b32_e32 v140, 7, v92
	v_lshl_add_u64 v[248:249], v[114:115], 0, v[140:141]
	global_load_dwordx4 v[164:167], v[248:249], off
	v_lshlrev_b32_e32 v140, 7, v93
	v_lshl_add_u64 v[250:251], v[114:115], 0, v[140:141]
	global_load_dwordx4 v[168:171], v[250:251], off
	v_lshlrev_b32_e32 v140, 7, v94
	v_lshl_add_u64 v[244:245], v[114:115], 0, v[140:141]
	global_load_dwordx4 v[172:175], v[244:245], off
	v_lshlrev_b32_e32 v140, 7, v95
	v_lshl_add_u64 v[246:247], v[114:115], 0, v[140:141]
	global_load_dwordx4 v[176:179], v[246:247], off
	v_lshlrev_b32_e32 v140, 7, v96
	v_lshl_add_u64 v[248:249], v[114:115], 0, v[140:141]
	global_load_dwordx4 v[180:183], v[248:249], off
	v_lshlrev_b32_e32 v140, 7, v97
	v_lshl_add_u64 v[250:251], v[114:115], 0, v[140:141]
	global_load_dwordx4 v[184:187], v[250:251], off
	v_lshlrev_b32_e32 v140, 7, v98
	v_lshl_add_u64 v[244:245], v[114:115], 0, v[140:141]
	global_load_dwordx4 v[188:191], v[244:245], off
	v_lshlrev_b32_e32 v140, 7, v99
	v_lshl_add_u64 v[246:247], v[114:115], 0, v[140:141]
	global_load_dwordx4 v[192:195], v[246:247], off
	v_lshlrev_b32_e32 v140, 7, v100
	v_lshl_add_u64 v[248:249], v[114:115], 0, v[140:141]
	global_load_dwordx4 v[196:199], v[248:249], off
	v_lshlrev_b32_e32 v140, 7, v101
	v_lshl_add_u64 v[250:251], v[114:115], 0, v[140:141]
	global_load_dwordx4 v[224:227], v[250:251], off
	v_lshlrev_b32_e32 v140, 7, v102
	v_lshl_add_u64 v[244:245], v[114:115], 0, v[140:141]
	global_load_dwordx4 v[228:231], v[244:245], off
	v_lshlrev_b32_e32 v140, 7, v103
	v_lshl_add_u64 v[246:247], v[114:115], 0, v[140:141]
	global_load_dwordx4 v[232:235], v[246:247], off
	v_lshlrev_b32_e32 v140, 7, v104
	v_lshl_add_u64 v[248:249], v[114:115], 0, v[140:141]
	global_load_dwordx4 v[236:239], v[248:249], off
	v_lshlrev_b32_e32 v140, 7, v105
	v_lshl_add_u64 v[250:251], v[114:115], 0, v[140:141]
	global_load_dwordx4 v[240:243], v[250:251], off
	s_waitcnt vmcnt(23)
	ds_write_b128 v37, v[2:5]
	s_waitcnt vmcnt(22)
	ds_write_b128 v37, v[6:9] offset:640
	s_waitcnt vmcnt(21)
	ds_write_b128 v37, v[10:13] offset:1312
	s_waitcnt vmcnt(20)
	ds_write_b128 v37, v[14:17] offset:1952
	v_lshlrev_b32_e32 v140, 7, v106
	v_lshl_add_u64 v[244:245], v[114:115], 0, v[140:141]
	global_load_dwordx4 v[2:5], v[244:245], off
	v_lshlrev_b32_e32 v140, 7, v107
	v_lshl_add_u64 v[246:247], v[114:115], 0, v[140:141]
	global_load_dwordx4 v[6:9], v[246:247], off
	v_lshlrev_b32_e32 v140, 7, v108
	v_lshl_add_u64 v[248:249], v[114:115], 0, v[140:141]
	global_load_dwordx4 v[10:13], v[248:249], off
	v_lshlrev_b32_e32 v140, 7, v109
	v_lshl_add_u64 v[250:251], v[114:115], 0, v[140:141]
	global_load_dwordx4 v[14:17], v[250:251], off
	s_waitcnt lgkmcnt(0)
	ds_read_b64_tr_b8 v[86:87], v36 offset:0
	ds_read_b64_tr_b8 v[88:89], v36 offset:16
	ds_read_b64_tr_b8 v[90:91], v36 offset:32
	ds_read_b64_tr_b8 v[92:93], v36 offset:48
	ds_read_b64_tr_b8 v[94:95], v36 offset:2624
	ds_read_b64_tr_b8 v[96:97], v36 offset:2640
	ds_read_b64_tr_b8 v[98:99], v36 offset:2656
	ds_read_b64_tr_b8 v[100:101], v36 offset:2672
	s_waitcnt lgkmcnt(0)
	s_waitcnt vmcnt(23)
	ds_write_b128 v37, v[38:41]
	s_waitcnt vmcnt(22)
	ds_write_b128 v37, v[42:45] offset:640
	s_waitcnt vmcnt(21)
	ds_write_b128 v37, v[46:49] offset:1312
	s_waitcnt vmcnt(20)
	ds_write_b128 v37, v[50:53] offset:1952
	v_lshlrev_b32_e32 v140, 7, v110
	v_lshl_add_u64 v[244:245], v[114:115], 0, v[140:141]
	global_load_dwordx4 v[38:41], v[244:245], off
	v_lshlrev_b32_e32 v140, 7, v111
	v_lshl_add_u64 v[246:247], v[114:115], 0, v[140:141]
	global_load_dwordx4 v[42:45], v[246:247], off
	v_lshlrev_b32_e32 v140, 7, v112
	v_lshl_add_u64 v[248:249], v[114:115], 0, v[140:141]
	global_load_dwordx4 v[46:49], v[248:249], off
	v_lshlrev_b32_e32 v140, 7, v113
	v_lshl_add_u64 v[250:251], v[114:115], 0, v[140:141]
	global_load_dwordx4 v[50:53], v[250:251], off
	v_mfma_f32_16x16x32_fp8_fp8 v[54:57], v[32:33], v[86:87], 0
	v_mfma_f32_16x16x32_fp8_fp8 v[58:61], v[32:33], v[88:89], 0
	v_mfma_f32_16x16x32_fp8_fp8 v[62:65], v[32:33], v[90:91], 0
	v_mfma_f32_16x16x32_fp8_fp8 v[66:69], v[32:33], v[92:93], 0
	v_mfma_f32_16x16x32_fp8_fp8 v[70:73], v[32:33], v[94:95], 0
	v_mfma_f32_16x16x32_fp8_fp8 v[74:77], v[32:33], v[96:97], 0
	v_mfma_f32_16x16x32_fp8_fp8 v[78:81], v[32:33], v[98:99], 0
	v_mfma_f32_16x16x32_fp8_fp8 v[82:85], v[32:33], v[100:101], 0
	s_waitcnt lgkmcnt(0)
	ds_read_b64_tr_b8 v[86:87], v36 offset:0
	ds_read_b64_tr_b8 v[88:89], v36 offset:16
	ds_read_b64_tr_b8 v[90:91], v36 offset:32
	ds_read_b64_tr_b8 v[92:93], v36 offset:48
	ds_read_b64_tr_b8 v[94:95], v36 offset:2624
	ds_read_b64_tr_b8 v[96:97], v36 offset:2640
	ds_read_b64_tr_b8 v[98:99], v36 offset:2656
	ds_read_b64_tr_b8 v[100:101], v36 offset:2672
	s_waitcnt lgkmcnt(0)
	s_waitcnt vmcnt(23)
	ds_write_b128 v37, v[156:159]
	s_waitcnt vmcnt(22)
	ds_write_b128 v37, v[160:163] offset:640
	s_waitcnt vmcnt(21)
	ds_write_b128 v37, v[164:167] offset:1312
	s_waitcnt vmcnt(20)
	ds_write_b128 v37, v[168:171] offset:1952
	v_mfma_f32_16x16x32_fp8_fp8 v[54:57], v[30:31], v[86:87], v[54:57]
	v_mfma_f32_16x16x32_fp8_fp8 v[58:61], v[30:31], v[88:89], v[58:61]
	v_mfma_f32_16x16x32_fp8_fp8 v[62:65], v[30:31], v[90:91], v[62:65]
	v_mfma_f32_16x16x32_fp8_fp8 v[66:69], v[30:31], v[92:93], v[66:69]
	v_mfma_f32_16x16x32_fp8_fp8 v[70:73], v[30:31], v[94:95], v[70:73]
	v_mfma_f32_16x16x32_fp8_fp8 v[74:77], v[30:31], v[96:97], v[74:77]
	v_mfma_f32_16x16x32_fp8_fp8 v[78:81], v[30:31], v[98:99], v[78:81]
	v_mfma_f32_16x16x32_fp8_fp8 v[82:85], v[30:31], v[100:101], v[82:85]
	s_waitcnt lgkmcnt(0)
	ds_read_b64_tr_b8 v[86:87], v36 offset:0
	ds_read_b64_tr_b8 v[88:89], v36 offset:16
	ds_read_b64_tr_b8 v[90:91], v36 offset:32
	ds_read_b64_tr_b8 v[92:93], v36 offset:48
	ds_read_b64_tr_b8 v[94:95], v36 offset:2624
	ds_read_b64_tr_b8 v[96:97], v36 offset:2640
	ds_read_b64_tr_b8 v[98:99], v36 offset:2656
	ds_read_b64_tr_b8 v[100:101], v36 offset:2672
	s_waitcnt lgkmcnt(0)
	s_waitcnt vmcnt(19)
	ds_write_b128 v37, v[172:175]
	s_waitcnt vmcnt(18)
	ds_write_b128 v37, v[176:179] offset:640
	s_waitcnt vmcnt(17)
	ds_write_b128 v37, v[180:183] offset:1312
	s_waitcnt vmcnt(16)
	ds_write_b128 v37, v[184:187] offset:1952
	v_mfma_f32_16x16x32_fp8_fp8 v[54:57], v[28:29], v[86:87], v[54:57]
	v_mfma_f32_16x16x32_fp8_fp8 v[58:61], v[28:29], v[88:89], v[58:61]
	v_mfma_f32_16x16x32_fp8_fp8 v[62:65], v[28:29], v[90:91], v[62:65]
	v_mfma_f32_16x16x32_fp8_fp8 v[66:69], v[28:29], v[92:93], v[66:69]
	v_mfma_f32_16x16x32_fp8_fp8 v[70:73], v[28:29], v[94:95], v[70:73]
	v_mfma_f32_16x16x32_fp8_fp8 v[74:77], v[28:29], v[96:97], v[74:77]
	v_mfma_f32_16x16x32_fp8_fp8 v[78:81], v[28:29], v[98:99], v[78:81]
	v_mfma_f32_16x16x32_fp8_fp8 v[82:85], v[28:29], v[100:101], v[82:85]
	s_waitcnt lgkmcnt(0)
	ds_read_b64_tr_b8 v[86:87], v36 offset:0
	ds_read_b64_tr_b8 v[88:89], v36 offset:16
	ds_read_b64_tr_b8 v[90:91], v36 offset:32
	ds_read_b64_tr_b8 v[92:93], v36 offset:48
	ds_read_b64_tr_b8 v[94:95], v36 offset:2624
	ds_read_b64_tr_b8 v[96:97], v36 offset:2640
	ds_read_b64_tr_b8 v[98:99], v36 offset:2656
	ds_read_b64_tr_b8 v[100:101], v36 offset:2672
	s_waitcnt lgkmcnt(0)
	s_waitcnt vmcnt(15)
	ds_write_b128 v37, v[188:191]
	s_waitcnt vmcnt(14)
	ds_write_b128 v37, v[192:195] offset:640
	s_waitcnt vmcnt(13)
	ds_write_b128 v37, v[196:199] offset:1312
	s_waitcnt vmcnt(12)
	ds_write_b128 v37, v[224:227] offset:1952
	v_mfma_f32_16x16x32_fp8_fp8 v[54:57], v[24:25], v[86:87], v[54:57]
	v_mfma_f32_16x16x32_fp8_fp8 v[58:61], v[24:25], v[88:89], v[58:61]
	v_mfma_f32_16x16x32_fp8_fp8 v[62:65], v[24:25], v[90:91], v[62:65]
	v_mfma_f32_16x16x32_fp8_fp8 v[66:69], v[24:25], v[92:93], v[66:69]
	v_mfma_f32_16x16x32_fp8_fp8 v[70:73], v[24:25], v[94:95], v[70:73]
	v_mfma_f32_16x16x32_fp8_fp8 v[74:77], v[24:25], v[96:97], v[74:77]
	v_mfma_f32_16x16x32_fp8_fp8 v[78:81], v[24:25], v[98:99], v[78:81]
	v_mfma_f32_16x16x32_fp8_fp8 v[82:85], v[24:25], v[100:101], v[82:85]
	s_waitcnt lgkmcnt(0)
	ds_read_b64_tr_b8 v[86:87], v36 offset:0
	ds_read_b64_tr_b8 v[88:89], v36 offset:16
	ds_read_b64_tr_b8 v[90:91], v36 offset:32
	ds_read_b64_tr_b8 v[92:93], v36 offset:48
	ds_read_b64_tr_b8 v[94:95], v36 offset:2624
	ds_read_b64_tr_b8 v[96:97], v36 offset:2640
	ds_read_b64_tr_b8 v[98:99], v36 offset:2656
	ds_read_b64_tr_b8 v[100:101], v36 offset:2672
	s_waitcnt lgkmcnt(0)
	s_waitcnt vmcnt(11)
	ds_write_b128 v37, v[228:231]
	s_waitcnt vmcnt(10)
	ds_write_b128 v37, v[232:235] offset:640
	s_waitcnt vmcnt(9)
	ds_write_b128 v37, v[236:239] offset:1312
	s_waitcnt vmcnt(8)
	ds_write_b128 v37, v[240:243] offset:1952
	v_mfma_f32_16x16x32_fp8_fp8 v[54:57], v[22:23], v[86:87], v[54:57]
	v_mfma_f32_16x16x32_fp8_fp8 v[58:61], v[22:23], v[88:89], v[58:61]
	v_mfma_f32_16x16x32_fp8_fp8 v[62:65], v[22:23], v[90:91], v[62:65]
	v_mfma_f32_16x16x32_fp8_fp8 v[66:69], v[22:23], v[92:93], v[66:69]
	v_mfma_f32_16x16x32_fp8_fp8 v[70:73], v[22:23], v[94:95], v[70:73]
	v_mfma_f32_16x16x32_fp8_fp8 v[74:77], v[22:23], v[96:97], v[74:77]
	v_mfma_f32_16x16x32_fp8_fp8 v[78:81], v[22:23], v[98:99], v[78:81]
	v_mfma_f32_16x16x32_fp8_fp8 v[82:85], v[22:23], v[100:101], v[82:85]
	s_waitcnt lgkmcnt(0)
	ds_read_b64_tr_b8 v[86:87], v36 offset:0
	ds_read_b64_tr_b8 v[88:89], v36 offset:16
	ds_read_b64_tr_b8 v[90:91], v36 offset:32
	ds_read_b64_tr_b8 v[92:93], v36 offset:48
	ds_read_b64_tr_b8 v[94:95], v36 offset:2624
	ds_read_b64_tr_b8 v[96:97], v36 offset:2640
	ds_read_b64_tr_b8 v[98:99], v36 offset:2656
	ds_read_b64_tr_b8 v[100:101], v36 offset:2672
	s_waitcnt lgkmcnt(0)
	s_waitcnt vmcnt(7)
	ds_write_b128 v37, v[2:5]
	s_waitcnt vmcnt(6)
	ds_write_b128 v37, v[6:9] offset:640
	s_waitcnt vmcnt(5)
	ds_write_b128 v37, v[10:13] offset:1312
	s_waitcnt vmcnt(4)
	ds_write_b128 v37, v[14:17] offset:1952
	v_mfma_f32_16x16x32_fp8_fp8 v[54:57], v[20:21], v[86:87], v[54:57]
	v_mfma_f32_16x16x32_fp8_fp8 v[58:61], v[20:21], v[88:89], v[58:61]
	v_mfma_f32_16x16x32_fp8_fp8 v[62:65], v[20:21], v[90:91], v[62:65]
	v_mfma_f32_16x16x32_fp8_fp8 v[66:69], v[20:21], v[92:93], v[66:69]
	v_mfma_f32_16x16x32_fp8_fp8 v[70:73], v[20:21], v[94:95], v[70:73]
	v_mfma_f32_16x16x32_fp8_fp8 v[74:77], v[20:21], v[96:97], v[74:77]
	v_mfma_f32_16x16x32_fp8_fp8 v[78:81], v[20:21], v[98:99], v[78:81]
	v_mfma_f32_16x16x32_fp8_fp8 v[82:85], v[20:21], v[100:101], v[82:85]
	s_waitcnt lgkmcnt(0)
	ds_read_b64_tr_b8 v[86:87], v36 offset:0
	ds_read_b64_tr_b8 v[88:89], v36 offset:16
	ds_read_b64_tr_b8 v[90:91], v36 offset:32
	ds_read_b64_tr_b8 v[92:93], v36 offset:48
	ds_read_b64_tr_b8 v[94:95], v36 offset:2624
	ds_read_b64_tr_b8 v[96:97], v36 offset:2640
	ds_read_b64_tr_b8 v[98:99], v36 offset:2656
	ds_read_b64_tr_b8 v[100:101], v36 offset:2672
	s_waitcnt lgkmcnt(0)
	s_waitcnt vmcnt(3)
	ds_write_b128 v37, v[38:41]
	s_waitcnt vmcnt(2)
	ds_write_b128 v37, v[42:45] offset:640
	s_waitcnt vmcnt(1)
	ds_write_b128 v37, v[46:49] offset:1312
	s_waitcnt vmcnt(0)
	ds_write_b128 v37, v[50:53] offset:1952
	v_mfma_f32_16x16x32_fp8_fp8 v[54:57], v[18:19], v[86:87], v[54:57]
	v_mfma_f32_16x16x32_fp8_fp8 v[58:61], v[18:19], v[88:89], v[58:61]
	v_mfma_f32_16x16x32_fp8_fp8 v[62:65], v[18:19], v[90:91], v[62:65]
	v_mfma_f32_16x16x32_fp8_fp8 v[66:69], v[18:19], v[92:93], v[66:69]
	v_mfma_f32_16x16x32_fp8_fp8 v[70:73], v[18:19], v[94:95], v[70:73]
	v_mfma_f32_16x16x32_fp8_fp8 v[74:77], v[18:19], v[96:97], v[74:77]
	v_mfma_f32_16x16x32_fp8_fp8 v[78:81], v[18:19], v[98:99], v[78:81]
	v_mfma_f32_16x16x32_fp8_fp8 v[82:85], v[18:19], v[100:101], v[82:85]
	s_waitcnt lgkmcnt(0)
	ds_read_b64_tr_b8 v[86:87], v36 offset:0
	ds_read_b64_tr_b8 v[88:89], v36 offset:16
	ds_read_b64_tr_b8 v[90:91], v36 offset:32
	ds_read_b64_tr_b8 v[92:93], v36 offset:48
	ds_read_b64_tr_b8 v[94:95], v36 offset:2624
	ds_read_b64_tr_b8 v[96:97], v36 offset:2640
	ds_read_b64_tr_b8 v[98:99], v36 offset:2656
	ds_read_b64_tr_b8 v[100:101], v36 offset:2672
	s_waitcnt lgkmcnt(0)
	v_mfma_f32_16x16x32_fp8_fp8 v[2:5], v[26:27], v[86:87], v[54:57]
	v_mfma_f32_16x16x32_fp8_fp8 v[6:9], v[26:27], v[88:89], v[58:61]
	v_mfma_f32_16x16x32_fp8_fp8 v[10:13], v[26:27], v[90:91], v[62:65]
	v_mfma_f32_16x16x32_fp8_fp8 v[14:17], v[26:27], v[92:93], v[66:69]
	v_mfma_f32_16x16x32_fp8_fp8 v[18:21], v[26:27], v[94:95], v[70:73]
	v_mfma_f32_16x16x32_fp8_fp8 v[22:25], v[26:27], v[96:97], v[74:77]
	v_mfma_f32_16x16x32_fp8_fp8 v[30:33], v[26:27], v[98:99], v[78:81]
	v_mfma_f32_16x16x32_fp8_fp8 v[26:29], v[26:27], v[100:101], v[82:85]
	v_div_scale_f32 v36, s[8:9], v35, v35, 1.0
	v_rcp_f32_e32 v37, v36
	v_readlane_b32 s8, v254, 62
	s_add_u32 s0, s8, s0
	v_readlane_b32 s8, v254, 63
	s_addc_u32 s1, s8, s1
	v_cmp_gt_i32_e64 s[8:9], 2, v211
	v_fma_f32 v38, -v36, v37, 1.0
	v_fmac_f32_e32 v37, v38, v37
	v_div_scale_f32 v38, vcc, 1.0, v35, 1.0
	v_mul_f32_e32 v39, v38, v37
	v_fma_f32 v40, -v36, v39, v38
	v_fmac_f32_e32 v39, v40, v37
	v_fma_f32 v36, -v36, v39, v38
	v_div_fmas_f32 v36, v36, v37, v39
	v_div_fixup_f32 v35, v36, v35, 1.0
	ds_bpermute_b32 v36, v34, v35
	ds_bpermute_b32 v37, v34, v35 offset:16
	v_cmp_eq_u32_e32 vcc, 0, v211
	s_and_saveexec_b64 s[10:11], s[8:9]
	s_cbranch_execz .LBB0_1336
	v_lshl_add_u32 v38, v211, 8, v210
	v_cndmask_b32_e32 v2, v18, v2, vcc
	s_waitcnt lgkmcnt(0)
	v_cndmask_b32_e32 v18, v37, v36, vcc
	v_mul_f32_e32 v2, v2, v18
	v_ashrrev_i32_e32 v39, 31, v38
	v_cvt_pk_bf16_f32 v2, v2, s0
	v_lshl_add_u64 v[36:37], v[38:39], 1, s[0:1]
	global_store_short v[36:37], v2, off
	v_cndmask_b32_e32 v2, v22, v6, vcc
	v_mul_f32_e32 v2, v2, v18
	v_cvt_pk_bf16_f32 v2, v2, s0
	global_store_short v[36:37], v2, off offset:32
	v_cndmask_b32_e32 v2, v30, v10, vcc
	v_mul_f32_e32 v2, v2, v18
	v_cvt_pk_bf16_f32 v2, v2, s0
	global_store_short v[36:37], v2, off offset:64
	v_cndmask_b32_e32 v2, v26, v14, vcc
	v_mul_f32_e32 v2, v2, v18
	v_cvt_pk_bf16_f32 v2, v2, s0
	global_store_short v[36:37], v2, off offset:96
